# grid barrier: leaders and followers poll the top arrival count itself (no generation-word hop) + early invalidate
# baseline (speedup 1.0000x reference)
; __device__ __forceinline__ unsigned xb_ld(unsigned* p)              { return __hip_atomic_load(p, __ATOMIC_RELAXED, __HIP_MEMORY_SCOPE_AGENT); }
; __device__ __forceinline__ unsigned xb_add(unsigned* p, unsigned v) { return __hip_atomic_fetch_add(p, v, __ATOMIC_RELAXED, __HIP_MEMORY_SCOPE_AGENT); }
; #define XB_SPIN(cond, bar) do { unsigned _sp = 0; while (cond) { __builtin_amdgcn_s_sleep(1); \
;     if ((++_sp & 255u) == 0u) { if (xb_ld(&(bar)[XB_TMO])) break; if (_sp > XB_SPIN_CAP) { atomicAdd(&(bar)[XB_TMO], 1u); break; } } } } while (0)
; __device__ __forceinline__ void xcd_barrier(const XcdBarrier& b) {
;     ...
;         const unsigned old = xb_add(&bar[XB_XSUB(b.x)], 1u);
;         const unsigned gen = old / nloc;
;         if (old + 1u == (gen + 1u) * nloc) {
;             __builtin_amdgcn_fence(__ATOMIC_RELEASE, "agent");
;             asm volatile("s_waitcnt vmcnt(0)" ::: "memory");
;             const unsigned og = xb_add(&bar[XB_TOP], 1u);
;             const unsigned tg = og / nx;
;             if (og + 1u == (tg + 1u) * nx) xb_add(&bar[XB_TOPGEN], 1u);
;             else XB_SPIN(xb_ld(&bar[XB_TOPGEN]) == tg, bar);
;             __builtin_amdgcn_fence(__ATOMIC_ACQUIRE, "agent");
;             xb_add(&bar[XB_XGEN(b.x)], 1u);
;             asm volatile("s_waitcnt vmcnt(0)" ::: "memory");
;         } else {
;             XB_SPIN(xb_ld(&bar[XB_XGEN(b.x)]) == gen, bar);
;             __builtin_amdgcn_fence(__ATOMIC_ACQUIRE, "agent");
.LBB0_244:
	s_or_b64 exec, exec, s[12:13]
	v_cvt_f32_u32_e32 v4, v2
	s_waitcnt vmcnt(0)
	v_readfirstlane_b32 s10, v3
	v_sub_u32_e32 v3, 0, v2
	v_rcp_iflag_f32_e32 v4, v4
	v_add_u32_e32 v5, s10, v1
	v_mul_f32_e32 v4, 0x4f7ffffe, v4
	v_cvt_u32_f32_e32 v4, v4
	v_mul_lo_u32 v1, v3, v4
	v_mul_hi_u32 v1, v4, v1
	v_add_u32_e32 v1, v4, v1
	v_mul_hi_u32 v1, v5, v1
	v_mul_lo_u32 v3, v1, v2
	v_sub_u32_e32 v3, v5, v3
	v_add_u32_e32 v4, 1, v1
	v_cmp_ge_u32_e32 vcc, v3, v2
	s_nop 1
	v_cndmask_b32_e32 v1, v1, v4, vcc
	v_sub_u32_e32 v4, v3, v2
	v_cndmask_b32_e32 v3, v3, v4, vcc
	v_add_u32_e32 v4, 1, v1
	v_cmp_ge_u32_e32 vcc, v3, v2
	v_add_u32_e32 v3, 1, v5
	s_nop 0
	v_cndmask_b32_e32 v1, v1, v4, vcc
	v_mul_lo_u32 v4, v2, v1
	v_add_u32_e32 v2, v4, v2
	v_cmp_ne_u32_e32 vcc, v3, v2
	s_and_saveexec_b64 s[10:11], vcc
	s_xor_b64 s[10:11], exec, s[10:11]
	s_cbranch_execz .LBB0_258
	buffer_inv sc1
	s_waitcnt lgkmcnt(0)
	v_add_u32_e32 v1, 1, v1
	v_mul_lo_u32 v1, v1, v0
	v_mov_b32_e32 v0, 0x7400
	global_load_dword v0, v0, s[0:1] sc1
	s_add_u32 s16, s0, 0x7400
	s_addc_u32 s17, s1, 0
	s_waitcnt vmcnt(0)
	v_cmp_gt_u32_e32 vcc, v1, v0
	s_and_saveexec_b64 s[12:13], vcc
	s_cbranch_execz .LBB0_257
	s_add_u32 s14, s0, 0x4200
	s_addc_u32 s15, s1, 0
	s_mov_b32 s28, 1
	s_mov_b64 s[18:19], 0
	v_mov_b32_e32 v0, 0
	s_branch .LBB0_248

.LBB0_252:
	global_load_dword v2, v0, s[16:17] sc1
	s_add_i32 s28, s28, 1
	s_mov_b64 s[24:25], -1
	s_waitcnt vmcnt(0)
	v_cmp_le_u32_e32 vcc, v1, v2
	s_orn2_b64 s[22:23], vcc, exec
	s_branch .LBB0_247

; __device__ __forceinline__ unsigned xb_ld(unsigned* p)              { return __hip_atomic_load(p, __ATOMIC_RELAXED, __HIP_MEMORY_SCOPE_AGENT); }
; __device__ __forceinline__ unsigned xb_add(unsigned* p, unsigned v) { return __hip_atomic_fetch_add(p, v, __ATOMIC_RELAXED, __HIP_MEMORY_SCOPE_AGENT); }
; #define XB_SPIN(cond, bar) do { unsigned _sp = 0; while (cond) { __builtin_amdgcn_s_sleep(1); \
;     if ((++_sp & 255u) == 0u) { if (xb_ld(&(bar)[XB_TMO])) break; if (_sp > XB_SPIN_CAP) { atomicAdd(&(bar)[XB_TMO], 1u); break; } } } } while (0)
; __device__ __forceinline__ void xcd_barrier(const XcdBarrier& b) {
;     ...
;             const unsigned og = xb_add(&bar[XB_TOP], 1u);
;             const unsigned tg = og / nx;
;             if (og + 1u == (tg + 1u) * nx) xb_add(&bar[XB_TOPGEN], 1u);
;             else XB_SPIN(xb_ld(&bar[XB_TOPGEN]) == tg, bar);
;             __builtin_amdgcn_fence(__ATOMIC_ACQUIRE, "agent");
.LBB0_261:
	s_or_b64 exec, exec, s[12:13]
	v_cvt_f32_u32_e32 v3, v0
	s_waitcnt vmcnt(0)
	v_readfirstlane_b32 s10, v2
	buffer_inv sc1
	s_add_u32 s12, s0, 0x7500
	s_addc_u32 s13, s1, 0
	v_rcp_iflag_f32_e32 v3, v3
	v_add_u32_e32 v1, s10, v1
	v_add_u32_e32 v4, 1, v1
	s_mov_b64 s[14:15], -1
	v_mul_f32_e32 v2, 0x4f7ffffe, v3
	v_cvt_u32_f32_e32 v2, v2
	v_sub_u32_e32 v3, 0, v0
	v_mul_lo_u32 v3, v3, v2
	v_mul_hi_u32 v3, v2, v3
	v_add_u32_e32 v2, v2, v3
	v_mul_hi_u32 v2, v1, v2
	v_mul_lo_u32 v3, v2, v0
	v_sub_u32_e32 v1, v1, v3
	v_add_u32_e32 v5, 1, v2
	v_cmp_ge_u32_e32 vcc, v1, v0
	v_sub_u32_e32 v3, v1, v0
	s_nop 0
	v_cndmask_b32_e32 v2, v2, v5, vcc
	v_cndmask_b32_e32 v1, v1, v3, vcc
	v_add_u32_e32 v3, 1, v2
	v_cmp_ge_u32_e32 vcc, v1, v0
	s_nop 1
	v_cndmask_b32_e32 v2, v2, v3, vcc
	v_mul_lo_u32 v1, v0, v2
	v_add_u32_e32 v0, v1, v0
	v_cmp_ne_u32_e32 vcc, v4, v0
	v_mov_b32_e32 v5, v0
	v_mov_b64_e32 v[0:1], s[12:13]
	s_and_saveexec_b64 s[10:11], vcc
	s_cbranch_execz .LBB0_273
	v_mov_b32_e32 v0, 0
	global_load_dword v1, v0, s[12:13] offset:-256 sc1
	s_mov_b64 s[18:19], 0
	s_waitcnt vmcnt(0)
	v_cmp_gt_u32_e32 vcc, v5, v1
	s_and_saveexec_b64 s[16:17], vcc
	s_cbranch_execz .LBB0_272
	s_add_u32 s14, s0, 0x4200
	s_addc_u32 s15, s1, 0
	s_mov_b32 s28, 1
	s_branch .LBB0_265

.LBB0_269:
	global_load_dword v1, v0, s[12:13] offset:-256 sc1
	s_add_i32 s28, s28, 1
	s_mov_b64 s[22:23], -1
	s_waitcnt vmcnt(0)
	v_cmp_le_u32_e32 vcc, v5, v1
	s_orn2_b64 s[26:27], vcc, exec
	s_branch .LBB0_264

; __device__ __forceinline__ unsigned xb_ld(unsigned* p)              { return __hip_atomic_load(p, __ATOMIC_RELAXED, __HIP_MEMORY_SCOPE_AGENT); }
; __device__ __forceinline__ unsigned xb_add(unsigned* p, unsigned v) { return __hip_atomic_fetch_add(p, v, __ATOMIC_RELAXED, __HIP_MEMORY_SCOPE_AGENT); }
; #define XB_SPIN(cond, bar) do { unsigned _sp = 0; while (cond) { __builtin_amdgcn_s_sleep(1); \
;     if ((++_sp & 255u) == 0u) { if (xb_ld(&(bar)[XB_TMO])) break; if (_sp > XB_SPIN_CAP) { atomicAdd(&(bar)[XB_TMO], 1u); break; } } } } while (0)
; __device__ __forceinline__ void xcd_barrier(const XcdBarrier& b) {
;     ...
;         const unsigned old = xb_add(&bar[XB_XSUB(b.x)], 1u);
;         const unsigned gen = old / nloc;
;         if (old + 1u == (gen + 1u) * nloc) {
;             __builtin_amdgcn_fence(__ATOMIC_RELEASE, "agent");
;             asm volatile("s_waitcnt vmcnt(0)" ::: "memory");
;             const unsigned og = xb_add(&bar[XB_TOP], 1u);
;             const unsigned tg = og / nx;
;             if (og + 1u == (tg + 1u) * nx) xb_add(&bar[XB_TOPGEN], 1u);
;             else XB_SPIN(xb_ld(&bar[XB_TOPGEN]) == tg, bar);
;             __builtin_amdgcn_fence(__ATOMIC_ACQUIRE, "agent");
;             xb_add(&bar[XB_XGEN(b.x)], 1u);
;             asm volatile("s_waitcnt vmcnt(0)" ::: "memory");
;         } else {
;             XB_SPIN(xb_ld(&bar[XB_XGEN(b.x)]) == gen, bar);
;             __builtin_amdgcn_fence(__ATOMIC_ACQUIRE, "agent");
.LBB0_470:
	s_or_b64 exec, exec, s[36:37]
	v_cvt_f32_u32_e32 v5, v3
	s_waitcnt vmcnt(0)
	v_readfirstlane_b32 s7, v4
	v_sub_u32_e32 v4, 0, v3
	v_rcp_iflag_f32_e32 v5, v5
	v_add_u32_e32 v6, s7, v0
	v_mul_f32_e32 v5, 0x4f7ffffe, v5
	v_cvt_u32_f32_e32 v5, v5
	v_mul_lo_u32 v0, v4, v5
	v_mul_hi_u32 v0, v5, v0
	v_add_u32_e32 v0, v5, v0
	v_mul_hi_u32 v0, v6, v0
	v_mul_lo_u32 v4, v0, v3
	v_sub_u32_e32 v4, v6, v4
	v_add_u32_e32 v5, 1, v0
	v_cmp_ge_u32_e32 vcc, v4, v3
	s_nop 1
	v_cndmask_b32_e32 v0, v0, v5, vcc
	v_sub_u32_e32 v5, v4, v3
	v_cndmask_b32_e32 v4, v4, v5, vcc
	v_add_u32_e32 v5, 1, v0
	v_cmp_ge_u32_e32 vcc, v4, v3
	v_add_u32_e32 v4, 1, v6
	s_nop 0
	v_cndmask_b32_e32 v0, v0, v5, vcc
	v_mul_lo_u32 v5, v3, v0
	v_add_u32_e32 v3, v5, v3
	v_cmp_ne_u32_e32 vcc, v4, v3
	s_and_saveexec_b64 s[8:9], vcc
	s_xor_b64 s[36:37], exec, s[8:9]
	s_cbranch_execz .LBB0_484
	buffer_inv sc1
	v_readlane_b32 s8, v252, 6
	v_readlane_b32 s9, v252, 7
	s_waitcnt lgkmcnt(0)
	v_add_u32_e32 v0, 1, v0
	v_mul_lo_u32 v0, v0, v2
	s_nop 3
	global_load_dword v2, v1, s[8:9] sc1
	s_waitcnt vmcnt(0)
	v_cmp_gt_u32_e32 vcc, v0, v2
	s_and_saveexec_b64 s[38:39], vcc
	s_cbranch_execz .LBB0_483
	s_mov_b32 s7, 1
	s_mov_b64 s[40:41], 0
	s_branch .LBB0_474

.LBB0_478:
	v_readlane_b32 s8, v252, 6
	v_readlane_b32 s9, v252, 7
	s_add_i32 s7, s7, 1
	s_mov_b64 s[52:53], -1
	s_nop 2
	global_load_dword v2, v1, s[8:9] sc1
	s_waitcnt vmcnt(0)
	v_cmp_le_u32_e32 vcc, v0, v2
	s_orn2_b64 s[50:51], vcc, exec
	s_branch .LBB0_473

; __device__ __forceinline__ unsigned xb_ld(unsigned* p)              { return __hip_atomic_load(p, __ATOMIC_RELAXED, __HIP_MEMORY_SCOPE_AGENT); }
; __device__ __forceinline__ unsigned xb_add(unsigned* p, unsigned v) { return __hip_atomic_fetch_add(p, v, __ATOMIC_RELAXED, __HIP_MEMORY_SCOPE_AGENT); }
; #define XB_SPIN(cond, bar) do { unsigned _sp = 0; while (cond) { __builtin_amdgcn_s_sleep(1); \
;     if ((++_sp & 255u) == 0u) { if (xb_ld(&(bar)[XB_TMO])) break; if (_sp > XB_SPIN_CAP) { atomicAdd(&(bar)[XB_TMO], 1u); break; } } } } while (0)
; __device__ __forceinline__ void xcd_barrier(const XcdBarrier& b) {
;     ...
;             const unsigned og = xb_add(&bar[XB_TOP], 1u);
;             const unsigned tg = og / nx;
;             if (og + 1u == (tg + 1u) * nx) xb_add(&bar[XB_TOPGEN], 1u);
;             else XB_SPIN(xb_ld(&bar[XB_TOPGEN]) == tg, bar);
;             __builtin_amdgcn_fence(__ATOMIC_ACQUIRE, "agent");
.LBB0_487:
	s_or_b64 exec, exec, s[38:39]
	s_waitcnt vmcnt(0)
	v_readfirstlane_b32 s7, v3
	buffer_inv sc1
	v_sub_u32_e32 v4, 0, v2
	v_readlane_b32 s8, v252, 8
	v_add_u32_e32 v3, s7, v0
	v_cvt_f32_u32_e32 v0, v2
	v_readlane_b32 s9, v252, 9
	s_mov_b64 s[38:39], -1
	v_rcp_iflag_f32_e32 v0, v0
	s_nop 0
	v_mul_f32_e32 v0, 0x4f7ffffe, v0
	v_cvt_u32_f32_e32 v0, v0
	v_mul_lo_u32 v4, v4, v0
	v_mul_hi_u32 v4, v0, v4
	v_add_u32_e32 v0, v0, v4
	v_mul_hi_u32 v0, v3, v0
	v_mul_lo_u32 v4, v0, v2
	v_sub_u32_e32 v4, v3, v4
	v_cmp_ge_u32_e32 vcc, v4, v2
	v_add_u32_e32 v5, 1, v0
	v_add_u32_e32 v3, 1, v3
	v_cndmask_b32_e32 v0, v0, v5, vcc
	v_sub_u32_e32 v5, v4, v2
	v_cndmask_b32_e32 v4, v4, v5, vcc
	v_cmp_ge_u32_e32 vcc, v4, v2
	v_add_u32_e32 v4, 1, v0
	s_nop 0
	v_cndmask_b32_e32 v0, v0, v4, vcc
	v_mul_lo_u32 v4, v2, v0
	v_add_u32_e32 v2, v4, v2
	v_cmp_ne_u32_e32 vcc, v3, v2
	v_mov_b32_e32 v5, v2
	v_mov_b64_e32 v[2:3], s[8:9]
	s_and_saveexec_b64 s[36:37], vcc
	s_cbranch_execz .LBB0_499
	v_readlane_b32 s8, v252, 6
	v_readlane_b32 s9, v252, 7
	s_mov_b64 s[40:41], 0
	s_nop 3
	global_load_dword v2, v1, s[8:9] sc1
	s_waitcnt vmcnt(0)
	v_cmp_gt_u32_e32 vcc, v5, v2
	s_and_saveexec_b64 s[38:39], vcc
	s_cbranch_execz .LBB0_498
	s_mov_b32 s7, 1
	s_branch .LBB0_491

.LBB0_495:
	v_readlane_b32 s8, v252, 6
	v_readlane_b32 s9, v252, 7
	s_add_i32 s7, s7, 1
	s_mov_b64 s[52:53], -1
	s_nop 2
	global_load_dword v2, v1, s[8:9] sc1
	s_waitcnt vmcnt(0)
	v_cmp_le_u32_e32 vcc, v5, v2
	s_orn2_b64 s[50:51], vcc, exec
	s_branch .LBB0_490

; __device__ __forceinline__ unsigned xb_ld(unsigned* p)              { return __hip_atomic_load(p, __ATOMIC_RELAXED, __HIP_MEMORY_SCOPE_AGENT); }
; __device__ __forceinline__ unsigned xb_add(unsigned* p, unsigned v) { return __hip_atomic_fetch_add(p, v, __ATOMIC_RELAXED, __HIP_MEMORY_SCOPE_AGENT); }
; #define XB_SPIN(cond, bar) do { unsigned _sp = 0; while (cond) { __builtin_amdgcn_s_sleep(1); \
;     if ((++_sp & 255u) == 0u) { if (xb_ld(&(bar)[XB_TMO])) break; if (_sp > XB_SPIN_CAP) { atomicAdd(&(bar)[XB_TMO], 1u); break; } } } } while (0)
; __device__ __forceinline__ void xcd_barrier(const XcdBarrier& b) {
;     ...
;         const unsigned old = xb_add(&bar[XB_XSUB(b.x)], 1u);
;         const unsigned gen = old / nloc;
;         if (old + 1u == (gen + 1u) * nloc) {
;             __builtin_amdgcn_fence(__ATOMIC_RELEASE, "agent");
;             asm volatile("s_waitcnt vmcnt(0)" ::: "memory");
;             const unsigned og = xb_add(&bar[XB_TOP], 1u);
;             const unsigned tg = og / nx;
;             if (og + 1u == (tg + 1u) * nx) xb_add(&bar[XB_TOPGEN], 1u);
;             else XB_SPIN(xb_ld(&bar[XB_TOPGEN]) == tg, bar);
;             __builtin_amdgcn_fence(__ATOMIC_ACQUIRE, "agent");
;             xb_add(&bar[XB_XGEN(b.x)], 1u);
;             asm volatile("s_waitcnt vmcnt(0)" ::: "memory");
;         } else {
;             XB_SPIN(xb_ld(&bar[XB_XGEN(b.x)]) == gen, bar);
;             __builtin_amdgcn_fence(__ATOMIC_ACQUIRE, "agent");
.LBB0_736:
	s_or_b64 exec, exec, s[36:37]
	v_cvt_f32_u32_e32 v5, v3
	s_waitcnt vmcnt(0)
	v_readfirstlane_b32 s6, v4
	v_sub_u32_e32 v4, 0, v3
	v_rcp_iflag_f32_e32 v5, v5
	v_add_u32_e32 v6, s6, v0
	v_mul_f32_e32 v5, 0x4f7ffffe, v5
	v_cvt_u32_f32_e32 v5, v5
	v_mul_lo_u32 v0, v4, v5
	v_mul_hi_u32 v0, v5, v0
	v_add_u32_e32 v0, v5, v0
	v_mul_hi_u32 v0, v6, v0
	v_mul_lo_u32 v4, v0, v3
	v_sub_u32_e32 v4, v6, v4
	v_add_u32_e32 v5, 1, v0
	v_cmp_ge_u32_e32 vcc, v4, v3
	s_nop 1
	v_cndmask_b32_e32 v0, v0, v5, vcc
	v_sub_u32_e32 v5, v4, v3
	v_cndmask_b32_e32 v4, v4, v5, vcc
	v_add_u32_e32 v5, 1, v0
	v_cmp_ge_u32_e32 vcc, v4, v3
	v_add_u32_e32 v4, 1, v6
	s_nop 0
	v_cndmask_b32_e32 v0, v0, v5, vcc
	v_mul_lo_u32 v5, v3, v0
	v_add_u32_e32 v3, v5, v3
	v_cmp_ne_u32_e32 vcc, v4, v3
	s_and_saveexec_b64 s[6:7], vcc
	s_xor_b64 s[36:37], exec, s[6:7]
	s_cbranch_execz .LBB0_750
	buffer_inv sc1
	v_readlane_b32 s6, v252, 6
	v_readlane_b32 s7, v252, 7
	s_waitcnt lgkmcnt(0)
	v_add_u32_e32 v0, 1, v0
	v_mul_lo_u32 v0, v0, v2
	s_nop 3
	global_load_dword v2, v1, s[6:7] sc1
	s_waitcnt vmcnt(0)
	v_cmp_gt_u32_e32 vcc, v0, v2
	s_and_saveexec_b64 s[38:39], vcc
	s_cbranch_execz .LBB0_749
	s_mov_b32 s6, 1
	s_mov_b64 s[40:41], 0
	s_branch .LBB0_740

.LBB0_744:
	v_readlane_b32 s8, v252, 6
	v_readlane_b32 s9, v252, 7
	s_add_i32 s6, s6, 1
	s_mov_b64 s[52:53], -1
	s_nop 2
	global_load_dword v2, v1, s[8:9] sc1
	s_waitcnt vmcnt(0)
	v_cmp_le_u32_e32 vcc, v0, v2
	s_orn2_b64 s[50:51], vcc, exec
	s_branch .LBB0_739

; __device__ __forceinline__ unsigned xb_ld(unsigned* p)              { return __hip_atomic_load(p, __ATOMIC_RELAXED, __HIP_MEMORY_SCOPE_AGENT); }
; __device__ __forceinline__ unsigned xb_add(unsigned* p, unsigned v) { return __hip_atomic_fetch_add(p, v, __ATOMIC_RELAXED, __HIP_MEMORY_SCOPE_AGENT); }
; #define XB_SPIN(cond, bar) do { unsigned _sp = 0; while (cond) { __builtin_amdgcn_s_sleep(1); \
;     if ((++_sp & 255u) == 0u) { if (xb_ld(&(bar)[XB_TMO])) break; if (_sp > XB_SPIN_CAP) { atomicAdd(&(bar)[XB_TMO], 1u); break; } } } } while (0)
; __device__ __forceinline__ void xcd_barrier(const XcdBarrier& b) {
;     ...
;             const unsigned og = xb_add(&bar[XB_TOP], 1u);
;             const unsigned tg = og / nx;
;             if (og + 1u == (tg + 1u) * nx) xb_add(&bar[XB_TOPGEN], 1u);
;             else XB_SPIN(xb_ld(&bar[XB_TOPGEN]) == tg, bar);
;             __builtin_amdgcn_fence(__ATOMIC_ACQUIRE, "agent");
.LBB0_753:
	s_or_b64 exec, exec, s[38:39]
	s_waitcnt vmcnt(0)
	v_readfirstlane_b32 s6, v3
	buffer_inv sc1
	v_sub_u32_e32 v4, 0, v2
	s_mov_b64 s[38:39], -1
	v_add_u32_e32 v3, s6, v0
	v_cvt_f32_u32_e32 v0, v2
	v_readlane_b32 s6, v252, 8
	v_readlane_b32 s7, v252, 9
	v_rcp_iflag_f32_e32 v0, v0
	s_nop 0
	v_mul_f32_e32 v0, 0x4f7ffffe, v0
	v_cvt_u32_f32_e32 v0, v0
	v_mul_lo_u32 v4, v4, v0
	v_mul_hi_u32 v4, v0, v4
	v_add_u32_e32 v0, v0, v4
	v_mul_hi_u32 v0, v3, v0
	v_mul_lo_u32 v4, v0, v2
	v_sub_u32_e32 v4, v3, v4
	v_cmp_ge_u32_e32 vcc, v4, v2
	v_add_u32_e32 v5, 1, v0
	v_add_u32_e32 v3, 1, v3
	v_cndmask_b32_e32 v0, v0, v5, vcc
	v_sub_u32_e32 v5, v4, v2
	v_cndmask_b32_e32 v4, v4, v5, vcc
	v_cmp_ge_u32_e32 vcc, v4, v2
	v_add_u32_e32 v4, 1, v0
	s_nop 0
	v_cndmask_b32_e32 v0, v0, v4, vcc
	v_mul_lo_u32 v4, v2, v0
	v_add_u32_e32 v2, v4, v2
	v_cmp_ne_u32_e32 vcc, v3, v2
	v_mov_b32_e32 v5, v2
	v_mov_b64_e32 v[2:3], s[6:7]
	s_and_saveexec_b64 s[36:37], vcc
	s_cbranch_execz .LBB0_765
	v_readlane_b32 s6, v252, 6
	v_readlane_b32 s7, v252, 7
	s_mov_b64 s[40:41], 0
	s_nop 3
	global_load_dword v2, v1, s[6:7] sc1
	s_waitcnt vmcnt(0)
	v_cmp_gt_u32_e32 vcc, v5, v2
	s_and_saveexec_b64 s[38:39], vcc
	s_cbranch_execz .LBB0_764
	s_mov_b32 s6, 1
	s_branch .LBB0_757

.LBB0_761:
	v_readlane_b32 s8, v252, 6
	v_readlane_b32 s9, v252, 7
	s_add_i32 s6, s6, 1
	s_mov_b64 s[52:53], -1
	s_nop 2
	global_load_dword v2, v1, s[8:9] sc1
	s_waitcnt vmcnt(0)
	v_cmp_le_u32_e32 vcc, v5, v2
	s_orn2_b64 s[50:51], vcc, exec
	s_branch .LBB0_756

.LBB0_1031:
	v_readlane_b32 s8, v252, 6
	v_readlane_b32 s9, v252, 7
	s_add_i32 s7, s7, 1
	s_mov_b64 s[48:49], -1
	s_nop 2
	global_load_dword v2, v1, s[8:9] sc1
	s_waitcnt vmcnt(0)
	v_cmp_le_u32_e32 vcc, v0, v2
	s_orn2_b64 s[46:47], vcc, exec
	s_branch .LBB0_1026

.LBB0_1048:
	v_readlane_b32 s8, v252, 6
	v_readlane_b32 s9, v252, 7
	s_add_i32 s7, s7, 1
	s_mov_b64 s[48:49], -1
	s_nop 2
	global_load_dword v2, v1, s[8:9] sc1
	s_waitcnt vmcnt(0)
	v_cmp_le_u32_e32 vcc, v5, v2
	s_orn2_b64 s[46:47], vcc, exec
	s_branch .LBB0_1043

; __device__ __forceinline__ unsigned xb_ld(unsigned* p)              { return __hip_atomic_load(p, __ATOMIC_RELAXED, __HIP_MEMORY_SCOPE_AGENT); }
; __device__ __forceinline__ unsigned xb_add(unsigned* p, unsigned v) { return __hip_atomic_fetch_add(p, v, __ATOMIC_RELAXED, __HIP_MEMORY_SCOPE_AGENT); }
; #define XB_SPIN(cond, bar) do { unsigned _sp = 0; while (cond) { __builtin_amdgcn_s_sleep(1); \
;     if ((++_sp & 255u) == 0u) { if (xb_ld(&(bar)[XB_TMO])) break; if (_sp > XB_SPIN_CAP) { atomicAdd(&(bar)[XB_TMO], 1u); break; } } } } while (0)
; __device__ __forceinline__ void xcd_barrier(const XcdBarrier& b) {
;     ...
;         const unsigned old = xb_add(&bar[XB_XSUB(b.x)], 1u);
;         const unsigned gen = old / nloc;
;         if (old + 1u == (gen + 1u) * nloc) {
;             __builtin_amdgcn_fence(__ATOMIC_RELEASE, "agent");
;             asm volatile("s_waitcnt vmcnt(0)" ::: "memory");
;             const unsigned og = xb_add(&bar[XB_TOP], 1u);
;             const unsigned tg = og / nx;
;             if (og + 1u == (tg + 1u) * nx) xb_add(&bar[XB_TOPGEN], 1u);
;             else XB_SPIN(xb_ld(&bar[XB_TOPGEN]) == tg, bar);
;             __builtin_amdgcn_fence(__ATOMIC_ACQUIRE, "agent");
;             xb_add(&bar[XB_XGEN(b.x)], 1u);
;             asm volatile("s_waitcnt vmcnt(0)" ::: "memory");
;         } else {
;             XB_SPIN(xb_ld(&bar[XB_XGEN(b.x)]) == gen, bar);
;             __builtin_amdgcn_fence(__ATOMIC_ACQUIRE, "agent");
.LBB0_1341:
	s_or_b64 exec, exec, s[38:39]
	v_cvt_f32_u32_e32 v5, v3
	s_waitcnt vmcnt(0)
	v_readfirstlane_b32 s7, v4
	v_sub_u32_e32 v4, 0, v3
	v_rcp_iflag_f32_e32 v5, v5
	v_add_u32_e32 v6, s7, v0
	v_mul_f32_e32 v5, 0x4f7ffffe, v5
	v_cvt_u32_f32_e32 v5, v5
	v_mul_lo_u32 v0, v4, v5
	v_mul_hi_u32 v0, v5, v0
	v_add_u32_e32 v0, v5, v0
	v_mul_hi_u32 v0, v6, v0
	v_mul_lo_u32 v4, v0, v3
	v_sub_u32_e32 v4, v6, v4
	v_add_u32_e32 v5, 1, v0
	v_cmp_ge_u32_e32 vcc, v4, v3
	s_nop 1
	v_cndmask_b32_e32 v0, v0, v5, vcc
	v_sub_u32_e32 v5, v4, v3
	v_cndmask_b32_e32 v4, v4, v5, vcc
	v_add_u32_e32 v5, 1, v0
	v_cmp_ge_u32_e32 vcc, v4, v3
	v_add_u32_e32 v4, 1, v6
	s_nop 0
	v_cndmask_b32_e32 v0, v0, v5, vcc
	v_mul_lo_u32 v5, v3, v0
	v_add_u32_e32 v3, v5, v3
	v_cmp_ne_u32_e32 vcc, v4, v3
	s_and_saveexec_b64 s[8:9], vcc
	s_xor_b64 s[38:39], exec, s[8:9]
	s_cbranch_execz .LBB0_1355
	buffer_inv sc1
	v_readlane_b32 s8, v252, 6
	v_readlane_b32 s9, v252, 7
	s_waitcnt lgkmcnt(0)
	v_add_u32_e32 v0, 1, v0
	v_mul_lo_u32 v0, v0, v2
	s_nop 3
	global_load_dword v2, v1, s[8:9] sc1
	s_waitcnt vmcnt(0)
	v_cmp_gt_u32_e32 vcc, v0, v2
	s_and_saveexec_b64 s[40:41], vcc
	s_cbranch_execz .LBB0_1354
	s_mov_b32 s7, 1
	s_mov_b64 s[44:45], 0
	s_branch .LBB0_1345

.LBB0_1349:
	v_readlane_b32 s8, v252, 6
	v_readlane_b32 s9, v252, 7
	s_add_i32 s7, s7, 1
	s_mov_b64 s[50:51], -1
	s_nop 2
	global_load_dword v2, v1, s[8:9] sc1
	s_waitcnt vmcnt(0)
	v_cmp_le_u32_e32 vcc, v0, v2
	s_orn2_b64 s[48:49], vcc, exec
	s_branch .LBB0_1344

; __device__ __forceinline__ unsigned xb_ld(unsigned* p)              { return __hip_atomic_load(p, __ATOMIC_RELAXED, __HIP_MEMORY_SCOPE_AGENT); }
; __device__ __forceinline__ unsigned xb_add(unsigned* p, unsigned v) { return __hip_atomic_fetch_add(p, v, __ATOMIC_RELAXED, __HIP_MEMORY_SCOPE_AGENT); }
; #define XB_SPIN(cond, bar) do { unsigned _sp = 0; while (cond) { __builtin_amdgcn_s_sleep(1); \
;     if ((++_sp & 255u) == 0u) { if (xb_ld(&(bar)[XB_TMO])) break; if (_sp > XB_SPIN_CAP) { atomicAdd(&(bar)[XB_TMO], 1u); break; } } } } while (0)
; __device__ __forceinline__ void xcd_barrier(const XcdBarrier& b) {
;     ...
;             const unsigned og = xb_add(&bar[XB_TOP], 1u);
;             const unsigned tg = og / nx;
;             if (og + 1u == (tg + 1u) * nx) xb_add(&bar[XB_TOPGEN], 1u);
;             else XB_SPIN(xb_ld(&bar[XB_TOPGEN]) == tg, bar);
;             __builtin_amdgcn_fence(__ATOMIC_ACQUIRE, "agent");
.LBB0_1358:
	s_or_b64 exec, exec, s[40:41]
	s_waitcnt vmcnt(0)
	v_readfirstlane_b32 s7, v3
	buffer_inv sc1
	v_sub_u32_e32 v4, 0, v2
	v_readlane_b32 s8, v252, 8
	v_add_u32_e32 v3, s7, v0
	v_cvt_f32_u32_e32 v0, v2
	v_readlane_b32 s9, v252, 9
	s_mov_b64 s[40:41], -1
	v_rcp_iflag_f32_e32 v0, v0
	s_nop 0
	v_mul_f32_e32 v0, 0x4f7ffffe, v0
	v_cvt_u32_f32_e32 v0, v0
	v_mul_lo_u32 v4, v4, v0
	v_mul_hi_u32 v4, v0, v4
	v_add_u32_e32 v0, v0, v4
	v_mul_hi_u32 v0, v3, v0
	v_mul_lo_u32 v4, v0, v2
	v_sub_u32_e32 v4, v3, v4
	v_cmp_ge_u32_e32 vcc, v4, v2
	v_add_u32_e32 v5, 1, v0
	v_add_u32_e32 v3, 1, v3
	v_cndmask_b32_e32 v0, v0, v5, vcc
	v_sub_u32_e32 v5, v4, v2
	v_cndmask_b32_e32 v4, v4, v5, vcc
	v_cmp_ge_u32_e32 vcc, v4, v2
	v_add_u32_e32 v4, 1, v0
	s_nop 0
	v_cndmask_b32_e32 v0, v0, v4, vcc
	v_mul_lo_u32 v4, v2, v0
	v_add_u32_e32 v2, v4, v2
	v_cmp_ne_u32_e32 vcc, v3, v2
	v_mov_b32_e32 v5, v2
	v_mov_b64_e32 v[2:3], s[8:9]
	s_and_saveexec_b64 s[38:39], vcc
	s_cbranch_execz .LBB0_1370
	v_readlane_b32 s8, v252, 6
	v_readlane_b32 s9, v252, 7
	s_mov_b64 s[44:45], 0
	s_nop 3
	global_load_dword v2, v1, s[8:9] sc1
	s_waitcnt vmcnt(0)
	v_cmp_gt_u32_e32 vcc, v5, v2
	s_and_saveexec_b64 s[40:41], vcc
	s_cbranch_execz .LBB0_1369
	s_mov_b32 s7, 1
	s_branch .LBB0_1362

.LBB0_1366:
	v_readlane_b32 s8, v252, 6
	v_readlane_b32 s9, v252, 7
	s_add_i32 s7, s7, 1
	s_mov_b64 s[50:51], -1
	s_nop 2
	global_load_dword v2, v1, s[8:9] sc1
	s_waitcnt vmcnt(0)
	v_cmp_le_u32_e32 vcc, v5, v2
	s_orn2_b64 s[48:49], vcc, exec
	s_branch .LBB0_1361

.LBB0_1521:
	v_readlane_b32 s8, v252, 6
	v_readlane_b32 s9, v252, 7
	s_add_i32 s6, s6, 1
	s_mov_b64 s[48:49], -1
	s_nop 2
	global_load_dword v2, v1, s[8:9] sc1
	s_waitcnt vmcnt(0)
	v_cmp_le_u32_e32 vcc, v0, v2
	s_orn2_b64 s[46:47], vcc, exec
	s_branch .LBB0_1516

.LBB0_1538:
	v_readlane_b32 s8, v252, 6
	v_readlane_b32 s9, v252, 7
	s_add_i32 s6, s6, 1
	s_mov_b64 s[48:49], -1
	s_nop 2
	global_load_dword v2, v1, s[8:9] sc1
	s_waitcnt vmcnt(0)
	v_cmp_le_u32_e32 vcc, v5, v2
	s_orn2_b64 s[46:47], vcc, exec
	s_branch .LBB0_1533
